# memkv GEMM moved from phase 2 to idle blocks of phase 4, gates on all blocks
# speedup vs baseline: 1.0135x; 1.0135x over previous
.LBB0_396:
	s_cmp_lt_i32 s90, 3
	s_cselect_b64 s[4:5], -1, 0
	s_cmp_gt_i32 s91, 2
	s_cselect_b64 s[6:7], -1, 0
	s_and_b64 s[6:7], s[4:5], s[6:7]
	s_andn2_b64 vcc, exec, s[6:7]
	s_cbranch_vccnz .LBB0_423
	s_cmpk_lt_i32 s84, 0x41
	s_cselect_b64 s[4:5], -1, 0
	s_cmp_lt_i32 s2, 32
	s_cselect_b64 s[8:9], -1, 0
	s_or_b64 s[12:13], s[8:9], s[4:5]
	s_andn2_b64 vcc, exec, s[12:13]
	v_and_b32_e32 v1, 48, v0
	s_branch .LBB0_414
.Lmemkv_entry:
	s_lshr_b32 s14, s18, 6
	v_lshrrev_b32_e32 v2, 5, v0
	v_lshrrev_b32_e32 v4, 1, v0
	s_lshr_b32 s15, s18, 8
	s_lshl_b32 s3, s14, 10
	v_and_b32_e32 v2, 4, v2
	v_bfe_u32 v3, v0, 2, 2
	v_and_b32_e32 v4, 24, v4
	s_add_u32 s33, s82, 0x2400000
	v_or3_b32 v2, v2, v3, v4
	v_lshlrev_b32_e32 v3, 4, v0
	s_addc_u32 s44, s83, 0
	v_or_b32_e32 v10, 0x2000, v3
	s_add_u32 s45, s82, 0x6000000
	v_lshrrev_b32_e32 v4, 7, v10
	s_movk_i32 s8, 0x60
	s_addc_u32 s46, s83, 0
	v_and_or_b32 v5, v4, s8, v2
	v_bfe_u32 v13, v0, 2, 4
	s_movk_i32 s8, 0x70
	s_bfe_u32 s67, s72, 0x20002
	v_and_or_b32 v4, v4, s8, v13
	s_ashr_i32 s36, s72, 4
	s_and_b32 s66, s72, 3
	s_lshl_b32 s8, s67, 20
	s_add_u32 s38, s33, s8
	s_addc_u32 s39, s44, 0
	s_ashr_i32 s37, s36, 31
	s_lshl_b32 s12, s66, 20
	s_lshl_b64 s[8:9], s[36:37], 22
	s_add_u32 s8, s45, s8
	s_addc_u32 s9, s46, s9
	s_add_u32 s40, s8, s12
	v_and_b32_e32 v6, 32, v0
	s_addc_u32 s41, s9, 0
	v_bitop3_b32 v11, v3, v6, 48 bitop3:0x6c
	v_and_b32_e32 v12, 64, v0
	s_add_u32 s8, s40, 0x80000
	v_or_b32_e32 v3, v11, v12
	s_addc_u32 s9, s41, 0
	s_waitcnt lgkmcnt(0)
	v_lshl_or_b32 v132, v4, 12, v3
	v_lshrrev_b32_e32 v4, 3, v0
	s_add_u32 s12, s38, 0x80000
	v_and_or_b32 v2, v4, 32, v2
	s_addc_u32 s13, s39, 0
	s_add_i32 s47, s3, 0
	v_lshl_or_b32 v134, v2, 12, v3
	s_add_i32 m0, s47, 0x10000
	v_lshl_or_b32 v130, v5, 12, v3
	global_load_lds_dwordx4 v134, s[40:41]
	s_add_i32 m0, s47, 0x12000
	v_and_or_b32 v2, v4, 48, v13
	global_load_lds_dwordx4 v130, s[40:41]
	s_add_i32 m0, s47, 0x14000
	v_lshl_or_b32 v136, v2, 12, v3
	global_load_lds_dwordx4 v134, s[8:9]
	s_add_i32 m0, s47, 0x16000
	s_add_i32 s48, s47, 0x2000
	global_load_lds_dwordx4 v130, s[8:9]
	s_mov_b32 m0, s47
	s_add_i32 s49, s47, 0x4000
	global_load_lds_dwordx4 v136, s[38:39]
	s_mov_b32 m0, s48
	s_add_i32 s50, s47, 0x6000
	global_load_lds_dwordx4 v132, s[38:39]
	s_mov_b32 m0, s49
	v_mov_b32_e32 v139, 0
	global_load_lds_dwordx4 v136, s[12:13]
	s_mov_b32 m0, s50
	v_mov_b32_e32 v135, v139
	global_load_lds_dwordx4 v132, s[12:13]
	v_mov_b32_e32 v131, v139
	v_mov_b32_e32 v137, v139
	v_mov_b32_e32 v133, v139
	s_cmp_eq_u32 s15, 1
	s_mov_b32 s51, 0
	v_lshl_add_u64 v[2:3], s[40:41], 0, v[134:135]
	v_lshl_add_u64 v[4:5], s[40:41], 0, v[130:131]
	s_mov_b64 s[8:9], 0x80000
	v_lshl_add_u64 v[6:7], s[38:39], 0, v[136:137]
	s_cselect_b64 s[12:13], -1, 0
	s_cmp_lg_u32 s15, 1
	v_lshl_add_u64 v[8:9], s[38:39], 0, v[132:133]
	s_cbranch_scc1 .LBB0_401
	s_barrier

.LBB0_404:
	s_add_i32 s51, s51, 1
	s_mul_i32 s27, s51, s52
	s_add_i32 s27, s27, s72
	s_cmp_lt_i32 s27, 32
	s_cselect_b64 s[34:35], -1, 0
	s_cmp_gt_i32 s27, 31
	s_cbranch_scc1 .LBB0_406
	s_bfe_u32 s65, s27, 0x20002
	s_ashr_i32 s26, s27, 4
	s_and_b32 s64, s27, 3
	s_lshl_b32 s27, s65, 20
	s_add_u32 s28, s33, s27
	s_addc_u32 s29, s44, 0
	s_ashr_i32 s27, s26, 31
	s_lshl_b32 s37, s64, 20
	s_lshl_b64 s[30:31], s[26:27], 22
	s_add_u32 s27, s45, s30
	s_addc_u32 s31, s46, s31
	s_add_u32 s30, s27, s37
	s_addc_u32 s31, s31, 0

.LBB0_413:
	s_waitcnt vmcnt(0)
	s_barrier
	s_mov_b64 s[12:13], -1
	s_branch .LBB0_605
.LBB0_414:
	s_and_b64 s[4:5], s[4:5], exec
	s_mov_b32 s3, 0
	s_cmp_lt_i32 s2, s3
	s_cselect_b64 s[4:5], -1, 0
	s_sub_i32 s8, s2, s3
	s_lshl_b32 s8, s8, 3
	s_add_i32 s8, s8, s88
	s_cmpk_gt_u32 s8, 0x7ff
	s_cselect_b64 s[12:13], -1, 0
	s_or_b64 s[4:5], s[4:5], s[12:13]
	s_and_b64 vcc, exec, s[4:5]
	s_cbranch_vccnz .LBB0_423
	v_lshlrev_b32_e32 v2, 12, v0
	v_and_b32_e32 v54, 0xf000, v2
	v_mov_b32_e32 v55, 0
	v_lshlrev_b32_e32 v2, 1, v1
	v_mov_b32_e32 v3, v55
	v_lshl_add_u64 v[4:5], s[82:83], 0, v[54:55]
	v_and_b32_e32 v54, 48, v246
	s_sub_i32 s3, s84, s3
	v_lshl_add_u64 v[2:3], v[4:5], 0, v[2:3]
	s_mov_b64 s[4:5], 0x36800000
	v_lshl_add_u64 v[4:5], s[82:83], 0, v[54:55]
	s_mov_b64 s[14:15], 0x200000
	s_ashr_i32 s9, s8, 31
	s_lshl_b32 s12, s3, 3
	v_lshl_add_u64 v[56:57], v[2:3], 0, s[4:5]
	s_mov_b64 s[4:5], 0x1648000
	v_lshl_add_u64 v[62:63], v[4:5], 0, s[14:15]
	s_lshl_b64 s[14:15], s[8:9], 16
	v_lshlrev_b32_e32 v1, 1, v0
	v_and_b32_e32 v70, 15, v0
	v_lshrrev_b32_e32 v6, 4, v246
	v_lshl_add_u64 v[58:59], v[2:3], 0, s[4:5]
	s_mov_b64 s[4:5], 0x1658000
	s_add_u32 s14, s14, 0x36800100
	v_and_b32_e32 v1, 0x60, v1
	v_lshl_add_u64 v[60:61], v[2:3], 0, s[4:5]
	v_lshlrev_b32_e32 v2, 2, v6
	s_addc_u32 s15, s15, 0
	s_ashr_i32 s13, s12, 31
	v_lshl_or_b32 v54, v70, 12, v1
	v_cmp_ne_u32_e64 s[4:5], 3, v6
	s_lshl_b64 s[16:17], s[12:13], 16
	v_lshl_add_u64 v[64:65], s[82:83], 0, v[54:55]
	s_mov_b32 s3, 0x1648000
	s_mov_b64 s[18:19], 0x100
	v_lshlrev_b32_e32 v1, 2, v2
	s_branch .LBB0_417

.LBB0_535:
	s_cmp_lt_i32 s90, 5
	s_cselect_b64 s[6:7], -1, 0
	s_and_b64 s[12:13], s[6:7], s[4:5]
	s_andn2_b64 vcc, exec, s[12:13]
	s_cbranch_vccnz .LBB0_605
	s_cmpk_gt_i32 s87, 0xbf
	s_cbranch_scc0 .Lp4_main
	s_add_i32 s3, s87, 0xffffff40
	s_and_b32 s8, s3, 1
	s_cmp_lg_u32 s8, 0
	s_cbranch_scc1 .LBB0_605
	s_lshr_b32 s72, s3, 1
	v_readfirstlane_b32 s18, v0
	v_and_b32_e32 v1, 48, v0
	s_cmpk_lt_i32 s84, 0x41
	s_cselect_b64 s[4:5], -1, 0
	s_branch .Lmemkv_entry
.Lp4_main:
	s_add_u32 s14, s82, 0x62e00000
	s_addc_u32 s15, s83, 0
	s_add_u32 s16, s82, 0x1402000
	s_addc_u32 s17, s83, 0
	s_add_u32 s18, s82, 0x1403800
	s_addc_u32 s19, s83, 0
	s_add_u32 s3, s82, 0x1408000
	s_addc_u32 s30, s83, 0
	s_add_u32 s31, s82, 0x62e80000
	s_addc_u32 s33, s83, 0
	s_add_u32 s34, s82, 0x140a000
	v_cmp_gt_u32_e64 s[4:5], 64, v0
	v_lshl_add_u32 v1, v0, 2, 0
	v_cmp_eq_u32_e64 s[6:7], 0, v0
	v_cmp_gt_u32_e64 s[8:9], 16, v0
	s_addc_u32 s35, s83, 0
	v_mov_b32_e32 v146, 0x1405000
	s_mov_b32 s36, 0x3fb8aa3b
	s_mov_b32 s37, 0xc2ce8ed0
	s_mov_b32 s38, 0x42b17218
	v_lshlrev_b32_e32 v147, 4, v0
	v_mov_b32_e32 v135, 0
	s_mov_b32 s39, 0x10000
	s_mov_b32 s40, 0x20000
	s_mov_b32 s41, 0x30000
	s_mov_b32 s42, 0x40000
	s_mov_b32 s43, 0x50000
	s_mov_b32 s44, 0x60000
	s_mov_b32 s45, 0x70000
	s_mov_b32 s46, 0x5ff0000
	s_mov_b64 s[20:21], 0x80000
	s_movk_i32 s47, 0x1000
	s_mov_b64 s[22:23], 0x2000
	v_mov_b32_e32 v148, 0x7f800000
	s_mov_b32 s48, s87
	s_mov_b32 s49, s87
	s_branch .LBB0_539
